# layer-0 combine+LayerNorm row loop: gain/bias of all four column groups resident (second eight quads in registers the next phase writes before reading)
# baseline (speedup 1.0000x reference)
; #define CMB_META(mm, M) do { const int _e0 = tok_e[2 * (mm)], _e1 = tok_e[2 * (mm) + 1]; (M).p0 = (size_t)pblk[_e0] * 256 + tok_p[2 * (mm)]; (M).p1 = (size_t)pblk[_e1] * 256 + tok_p[2 * (mm) + 1]; \
;         (M).h0 = tok_g[2 * (mm)] * (1.0f / 16.0f); (M).h1 = tok_g[2 * (mm) + 1] * (1.0f / 16.0f); } while (0)
; #define CMB_ROWS(mm, M, R) do { _Pragma("unroll") for (int i = 0; i < 4; ++i) { const int col = 8 * lane + 512 * i; (R).xa[i] = *(const u32x4*)(x1b + (size_t)(mm) * DM + col); \
;         (R).ya[i] = *(const u32x2*)((const unsigned char*)Yr + (M).p0 * DM + col); (R).yb[i] = *(const u32x2*)((const unsigned char*)Yr + (M).p1 * DM + col); } } while (0)
; template <bool FINAL> ...
;     ...
;     const int mstep = G * 8, m0 = bid * 8 + wid;
;     Meta Mc, Mn; Rows Rc, Rn;
;     Mc.p0 = Mc.p1 = 0; Mc.h0 = Mc.h1 = 0.f; Mn = Mc;
;     if (m0 < T_) { CMB_META(m0, Mc); CMB_ROWS(m0, Mc, Rc); }
;     if (m0 + mstep < T_) CMB_META(m0 + mstep, Mn);
;     Rn = Rc;
;     ...
;             const f32x4 ga = *(const f32x4*)(g + col), gb = *(const f32x4*)(g + col + 4), ba = *(const f32x4*)(bb + col), bbv = *(const f32x4*)(bb + col + 4);
.LBB0_1104:
	s_andn2_b64 vcc, exec, s[6:7]
	s_cbranch_vccnz .LBB0_1111
	v_lshlrev_b32_e32 v232, 3, v4
	s_ashr_i32 s1, s0, 31
	v_lshl_add_u64 v[48:49], s[2:3], 0, v[232:233]
	s_lshl_b64 s[2:3], s[0:1], 11
	s_add_u32 s2, s40, s2
	s_addc_u32 s3, s41, s3
	v_lshl_add_u64 v[50:51], s[2:3], 0, v[232:233]
	s_lshl_b64 s[2:3], s[0:1], 12
	s_add_u32 s2, s42, s2
	v_readlane_b32 s1, v254, 50
	s_addc_u32 s3, s43, s3
	s_add_i32 s1, s1, s15
	s_lshl_b32 s34, s1, 1
	v_readlane_b32 s1, v254, 6
	s_add_i32 s6, s1, s15
	v_lshlrev_b32_e32 v6, 5, v4
	v_mov_b32_e32 v7, v233
	s_ashr_i32 s7, s6, 31
	v_lshl_add_u64 v[36:37], s[44:45], 0, v[6:7]
	v_lshl_add_u64 v[38:39], s[46:47], 0, v[6:7]
	v_or_b32_e32 v8, 0x1000, v6
	v_mov_b32_e32 v9, v233
	v_or_b32_e32 v6, 0x1800, v6
	s_lshl_b64 s[6:7], s[6:7], 12
	v_lshl_add_u64 v[40:41], s[44:45], 0, v[8:9]
	v_lshl_add_u64 v[42:43], s[46:47], 0, v[8:9]
	v_lshl_add_u64 v[44:45], s[44:45], 0, v[6:7]
	v_lshl_add_u64 v[46:47], s[46:47], 0, v[6:7]
	v_lshlrev_b32_e32 v232, 4, v4
	s_add_u32 s38, s42, s6
	s_waitcnt vmcnt(11)
	v_mov_b64_e32 v[4:5], v[32:33]
	s_waitcnt vmcnt(8)
	v_mov_b64_e32 v[8:9], v[28:29]
	s_waitcnt vmcnt(5)
	v_mov_b64_e32 v[12:13], v[24:25]
	s_waitcnt vmcnt(2)
	v_mov_b64_e32 v[16:17], v[20:21]
	s_addc_u32 s39, s43, s7
	v_mov_b64_e32 v[6:7], v[34:35]
	v_mov_b64_e32 v[10:11], v[30:31]
	v_mov_b64_e32 v[14:15], v[26:27]
	v_mov_b64_e32 v[18:19], v[22:23]
	v_mov_b64_e32 v[52:53], v[86:87]
	v_mov_b64_e32 v[54:55], v[82:83]
	v_mov_b64_e32 v[56:57], v[72:73]
	s_waitcnt vmcnt(1)
	v_mov_b64_e32 v[58:59], v[78:79]
	v_mov_b64_e32 v[60:61], v[88:89]
	v_mov_b64_e32 v[62:63], v[84:85]
	v_mov_b64_e32 v[64:65], v[74:75]
	s_waitcnt vmcnt(0)
	v_mov_b64_e32 v[68:69], v[80:81]
	global_load_dwordx4 v[176:179], v[36:37], off offset:16
	global_load_dwordx4 v[180:183], v[36:37], off
	global_load_dwordx4 v[184:187], v[38:39], off offset:16
	global_load_dwordx4 v[188:191], v[38:39], off
	global_load_dwordx4 v[192:195], v[36:37], off offset:2064
	global_load_dwordx4 v[196:199], v[36:37], off offset:2048
	global_load_dwordx4 v[200:203], v[38:39], off offset:2064
	global_load_dwordx4 v[212:215], v[38:39], off offset:2048
	global_load_dwordx4 v[144:147], v[40:41], off offset:16
	global_load_dwordx4 v[148:151], v[40:41], off
	global_load_dwordx4 v[152:155], v[42:43], off offset:16
	global_load_dwordx4 v[156:159], v[42:43], off
	global_load_dwordx4 v[160:163], v[44:45], off offset:16
	global_load_dwordx4 v[168:171], v[44:45], off
	global_load_dwordx4 v[172:175], v[46:47], off offset:16
	global_load_dwordx4 v[204:207], v[46:47], off
	s_branch .LBB0_1107
.LBB0_1106:
	v_cvt_pk_f32_fp8_e32 v[92:93], v86
	v_cvt_pk_f32_fp8_e32 v[94:95], v88
	v_lshlrev_b32_e32 v91, 16, v32
	v_and_b32_e32 v32, 0xffff0000, v32
	v_mov_b32_e32 v96, v92
	v_mov_b32_e32 v97, v94
	v_pk_mul_f32 v[96:97], v[76:77], v[96:97]
	v_mov_b32_e32 v94, v93
	v_fma_f32 v91, v90, v91, v96
	v_add_f32_e32 v91, v91, v97
	v_pk_mul_f32 v[92:93], v[76:77], v[94:95]
	v_cvt_pk_f32_fp8_sdwa v[94:95], v86 src0_sel:WORD_1
	v_cvt_pk_f32_fp8_sdwa v[96:97], v88 src0_sel:WORD_1
	v_fma_f32 v32, v90, v32, v92
	v_add_f32_e32 v92, v32, v93
	v_add_f32_e32 v32, v91, v92
	v_mov_b32_e32 v98, v94
	v_mov_b32_e32 v99, v96
	v_add_f32_e32 v93, 0, v32
	v_lshlrev_b32_e32 v32, 16, v33
	v_pk_mul_f32 v[98:99], v[76:77], v[98:99]
	v_mov_b32_e32 v96, v95
	v_fma_f32 v32, v90, v32, v98
	v_add_f32_e32 v86, v32, v99
	v_and_b32_e32 v88, 0xffff0000, v33
	v_pk_mul_f32 v[32:33], v[76:77], v[96:97]
	v_cvt_pk_f32_fp8_e32 v[94:95], v89
	v_fma_f32 v32, v90, v88, v32
	v_add_f32_e32 v88, v32, v33
	v_add_f32_e32 v32, v86, v88
	v_add_f32_e32 v98, v93, v32
	v_cvt_pk_f32_fp8_e32 v[32:33], v87
	v_mov_b32_e32 v97, v94
	v_lshlrev_b32_e32 v93, 16, v34
	v_and_b32_e32 v34, 0xffff0000, v34
	v_mov_b32_e32 v96, v32
	v_pk_mul_f32 v[96:97], v[76:77], v[96:97]
	v_mov_b32_e32 v94, v33
	v_fma_f32 v32, v90, v93, v96
	v_add_f32_e32 v93, v32, v97
	v_pk_mul_f32 v[32:33], v[76:77], v[94:95]
	v_cvt_pk_f32_fp8_sdwa v[96:97], v89 src0_sel:WORD_1
	v_fma_f32 v32, v90, v34, v32
	v_add_f32_e32 v95, v32, v33
	v_add_f32_e32 v32, v93, v95
	v_add_f32_e32 v34, v98, v32
	v_cvt_pk_f32_fp8_sdwa v[32:33], v87 src0_sel:WORD_1
	v_mov_b32_e32 v99, v96
	v_lshlrev_b32_e32 v87, 16, v35
	v_and_b32_e32 v35, 0xffff0000, v35
	v_mov_b32_e32 v98, v32
	v_pk_mul_f32 v[98:99], v[76:77], v[98:99]
	v_mov_b32_e32 v96, v33
	v_fma_f32 v32, v90, v87, v98
	v_add_f32_e32 v100, v32, v99
	v_pk_mul_f32 v[32:33], v[76:77], v[96:97]
	v_lshlrev_b32_e32 v89, 16, v28
	v_fma_f32 v32, v90, v35, v32
	v_add_f32_e32 v102, v32, v33
	v_add_f32_e32 v32, v100, v102
	v_add_f32_e32 v87, v34, v32
	v_cvt_pk_f32_fp8_e32 v[32:33], v82
	v_cvt_pk_f32_fp8_e32 v[34:35], v84
	v_and_b32_e32 v28, 0xffff0000, v28
	s_mov_b32 s0, 0x36600000
	v_mov_b32_e32 v96, v32
	v_mov_b32_e32 v97, v34
	v_mov_b32_e32 v34, v33
	v_pk_mul_f32 v[96:97], v[76:77], v[96:97]
	v_pk_mul_f32 v[34:35], v[76:77], v[34:35]
	v_fma_f32 v32, v90, v89, v96
	v_fma_f32 v28, v90, v28, v34
	v_add_f32_e32 v32, v32, v97
	v_add_f32_e32 v33, v28, v35
	v_cvt_pk_f32_fp8_sdwa v[34:35], v82 src0_sel:WORD_1
	v_cvt_pk_f32_fp8_sdwa v[96:97], v84 src0_sel:WORD_1
	v_add_f32_e32 v28, v32, v33
	v_add_f32_e32 v87, v87, v28
	v_mov_b32_e32 v98, v34
	v_mov_b32_e32 v99, v96
	v_lshlrev_b32_e32 v28, 16, v29
	v_pk_mul_f32 v[98:99], v[76:77], v[98:99]
	v_mov_b32_e32 v96, v35
	v_fma_f32 v28, v90, v28, v98
	v_add_f32_e32 v82, v28, v99
	v_and_b32_e32 v34, 0xffff0000, v29
	v_pk_mul_f32 v[28:29], v[76:77], v[96:97]
	s_nop 0
	v_fma_f32 v28, v90, v34, v28
	v_add_f32_e32 v84, v28, v29
	v_add_f32_e32 v28, v82, v84
	v_add_f32_e32 v94, v87, v28
	v_cvt_pk_f32_fp8_e32 v[28:29], v83
	v_cvt_pk_f32_fp8_e32 v[34:35], v85
; #define CMB_PAIR(j, W, SEL) do { const f32x2 a2 = __builtin_amdgcn_cvt_pk_f32_fp8((int)aw[W], SEL), b2 = __builtin_amdgcn_cvt_pk_f32_fp8((int)bw[W], SEL); \
;                     v[i * 8 + 2 * (j)] = ALPHA * bflo(xw[j]) + h0 * a2[0] + h1 * b2[0]; v[i * 8 + 2 * (j) + 1] = ALPHA * bfhi(xw[j]) + h0 * a2[1] + h1 * b2[1]; \
;                     s += v[i * 8 + 2 * (j)] + v[i * 8 + 2 * (j) + 1]; } while (0)
; template <bool FINAL> ...
;     ...
;         for (int i = 0; i < 4; ++i) {
;             const unsigned xw[4] = {Rc.xa[i].x, Rc.xa[i].y, Rc.xa[i].z, Rc.xa[i].w}; const unsigned aw[2] = {Rc.ya[i].x, Rc.ya[i].y}, bw[2] = {Rc.yb[i].x, Rc.yb[i].y};
;     ...
;             CMB_PAIR(0, 0, false); CMB_PAIR(1, 0, true); CMB_PAIR(2, 1, false); CMB_PAIR(3, 1, true);
;     ...
;         }
;         Mc = Mn; Mn = Mnn; Rc = Rn;
;         const float mean = wave_sum(s) * (1.0f / DM); float q = 0.f;
	v_lshlrev_b32_e32 v87, 16, v30
	v_and_b32_e32 v30, 0xffff0000, v30
	v_mov_b32_e32 v96, v28
	v_mov_b32_e32 v97, v34
	v_pk_mul_f32 v[96:97], v[76:77], v[96:97]
	v_mov_b32_e32 v34, v29
	v_fma_f32 v28, v90, v87, v96
	v_add_f32_e32 v87, v28, v97
	v_pk_mul_f32 v[28:29], v[76:77], v[34:35]
	v_cvt_pk_f32_fp8_sdwa v[34:35], v85 src0_sel:WORD_1
	v_fma_f32 v28, v90, v30, v28
	v_add_f32_e32 v89, v28, v29
	v_add_f32_e32 v28, v87, v89
	v_add_f32_e32 v30, v94, v28
	v_cvt_pk_f32_fp8_sdwa v[28:29], v83 src0_sel:WORD_1
	v_mov_b32_e32 v97, v34
	v_lshlrev_b32_e32 v83, 16, v31
	v_and_b32_e32 v31, 0xffff0000, v31
	v_mov_b32_e32 v96, v28
	v_pk_mul_f32 v[96:97], v[76:77], v[96:97]
	v_mov_b32_e32 v34, v29
	v_fma_f32 v28, v90, v83, v96
	v_add_f32_e32 v97, v28, v97
	v_pk_mul_f32 v[28:29], v[76:77], v[34:35]
	v_lshlrev_b32_e32 v85, 16, v24
	v_fma_f32 v28, v90, v31, v28
	v_add_f32_e32 v98, v28, v29
	v_add_f32_e32 v28, v97, v98
	v_add_f32_e32 v83, v30, v28
	v_cvt_pk_f32_fp8_e32 v[28:29], v72
	v_cvt_pk_f32_fp8_e32 v[30:31], v74
	v_and_b32_e32 v24, 0xffff0000, v24
	v_mov_b32_e32 v34, v28
	v_mov_b32_e32 v35, v30
	v_pk_mul_f32 v[34:35], v[76:77], v[34:35]
	v_mov_b32_e32 v30, v29
	v_fma_f32 v28, v90, v85, v34
	v_add_f32_e32 v34, v28, v35
	v_pk_mul_f32 v[28:29], v[76:77], v[30:31]
	v_cvt_pk_f32_fp8_sdwa v[30:31], v74 src0_sel:WORD_1
	v_fma_f32 v24, v90, v24, v28
	v_add_f32_e32 v35, v24, v29
	v_cvt_pk_f32_fp8_sdwa v[28:29], v72 src0_sel:WORD_1
	v_add_f32_e32 v24, v34, v35
	v_mov_b32_e32 v105, v30
	v_add_f32_e32 v85, v83, v24
	v_mov_b32_e32 v104, v28
	v_lshlrev_b32_e32 v24, 16, v25
	v_pk_mul_f32 v[104:105], v[76:77], v[104:105]
	v_mov_b32_e32 v30, v29
	v_fma_f32 v24, v90, v24, v104
	v_add_f32_e32 v74, v24, v105
	v_and_b32_e32 v28, 0xffff0000, v25
	v_pk_mul_f32 v[24:25], v[76:77], v[30:31]
	s_nop 0
	v_fma_f32 v24, v90, v28, v24
	v_add_f32_e32 v83, v24, v25
	v_add_f32_e32 v24, v74, v83
	v_add_f32_e32 v72, v85, v24
	v_cvt_pk_f32_fp8_e32 v[24:25], v73
	v_cvt_pk_f32_fp8_e32 v[28:29], v75
	v_lshlrev_b32_e32 v85, 16, v26
	v_and_b32_e32 v26, 0xffff0000, v26
	v_mov_b32_e32 v30, v24
	v_mov_b32_e32 v31, v28
	v_pk_mul_f32 v[30:31], v[76:77], v[30:31]
	v_mov_b32_e32 v28, v25
	v_fma_f32 v24, v90, v85, v30
	v_add_f32_e32 v85, v24, v31
	v_pk_mul_f32 v[24:25], v[76:77], v[28:29]
	v_cvt_pk_f32_fp8_sdwa v[28:29], v75 src0_sel:WORD_1
	v_fma_f32 v24, v90, v26, v24
	v_add_f32_e32 v94, v24, v25
	v_add_f32_e32 v24, v85, v94
	v_add_f32_e32 v26, v72, v24
	v_cvt_pk_f32_fp8_sdwa v[24:25], v73 src0_sel:WORD_1
	v_mov_b32_e32 v31, v28
	v_lshlrev_b32_e32 v72, 16, v27
	v_and_b32_e32 v27, 0xffff0000, v27
	v_mov_b32_e32 v30, v24
	v_pk_mul_f32 v[30:31], v[76:77], v[30:31]
	v_mov_b32_e32 v28, v25
	v_fma_f32 v24, v90, v72, v30
	v_add_f32_e32 v99, v24, v31
	v_pk_mul_f32 v[24:25], v[76:77], v[28:29]
	v_lshlrev_b32_e32 v31, 16, v20
	v_fma_f32 v24, v90, v27, v24
	v_add_f32_e32 v101, v24, v25
	v_add_f32_e32 v24, v99, v101
	v_add_f32_e32 v30, v26, v24
	v_cvt_pk_f32_fp8_e32 v[24:25], v78
	v_cvt_pk_f32_fp8_e32 v[26:27], v80
	v_and_b32_e32 v20, 0xffff0000, v20
	v_mov_b32_e32 v28, v24
	v_mov_b32_e32 v29, v26
	v_pk_mul_f32 v[28:29], v[76:77], v[28:29]
	v_mov_b32_e32 v26, v25
	v_fma_f32 v24, v90, v31, v28
	v_add_f32_e32 v72, v24, v29
	v_pk_mul_f32 v[24:25], v[76:77], v[26:27]
	v_cvt_pk_f32_fp8_sdwa v[26:27], v80 src0_sel:WORD_1
	v_fma_f32 v20, v90, v20, v24
	v_add_f32_e32 v73, v20, v25
	v_cvt_pk_f32_fp8_sdwa v[24:25], v78 src0_sel:WORD_1
	v_add_f32_e32 v20, v72, v73
	v_mov_b32_e32 v29, v26
	v_add_f32_e32 v30, v30, v20
	v_mov_b32_e32 v28, v24
	v_lshlrev_b32_e32 v20, 16, v21
	v_pk_mul_f32 v[28:29], v[76:77], v[28:29]
	v_mov_b32_e32 v26, v25
	v_fma_f32 v20, v90, v20, v28
	v_add_f32_e32 v75, v20, v29
	v_and_b32_e32 v24, 0xffff0000, v21
	v_pk_mul_f32 v[20:21], v[76:77], v[26:27]
	v_lshlrev_b32_e32 v29, 16, v22
	v_fma_f32 v20, v90, v24, v20
	v_add_f32_e32 v78, v20, v21
	v_add_f32_e32 v20, v75, v78
	v_add_f32_e32 v28, v30, v20
	v_cvt_pk_f32_fp8_e32 v[20:21], v79
	v_cvt_pk_f32_fp8_e32 v[24:25], v81
	v_and_b32_e32 v22, 0xffff0000, v22
	v_mov_b32_e32 v26, v20
	v_mov_b32_e32 v27, v24
	v_pk_mul_f32 v[26:27], v[76:77], v[26:27]
	v_mov_b32_e32 v24, v21
	v_fma_f32 v20, v90, v29, v26
	v_add_f32_e32 v80, v20, v27
	v_pk_mul_f32 v[20:21], v[76:77], v[24:25]
	v_cvt_pk_f32_fp8_sdwa v[24:25], v81 src0_sel:WORD_1
	v_fma_f32 v20, v90, v22, v20
	v_add_f32_e32 v96, v20, v21
	v_add_f32_e32 v20, v80, v96
	v_add_f32_e32 v22, v28, v20
	v_cvt_pk_f32_fp8_sdwa v[20:21], v79 src0_sel:WORD_1
	v_mov_b32_e32 v27, v24
	v_lshlrev_b32_e32 v28, 16, v23
	v_and_b32_e32 v23, 0xffff0000, v23
	v_mov_b32_e32 v26, v20
	v_pk_mul_f32 v[26:27], v[76:77], v[26:27]
	v_mov_b32_e32 v24, v21
	v_fma_f32 v20, v90, v28, v26
	v_add_f32_e32 v79, v20, v27
	v_pk_mul_f32 v[20:21], v[76:77], v[24:25]
	s_nop 0
	v_fma_f32 v20, v90, v23, v20
	v_add_f32_e32 v76, v20, v21
	v_add_f32_e32 v20, v79, v76
	v_add_f32_e32 v20, v22, v20
	ds_swizzle_b32 v21, v20 offset:swizzle(SWAP,1)
	s_waitcnt lgkmcnt(0)
	v_add_f32_e32 v20, v20, v21
	ds_swizzle_b32 v21, v20 offset:swizzle(SWAP,2)
	s_waitcnt lgkmcnt(0)
	v_add_f32_e32 v20, v20, v21
	ds_swizzle_b32 v21, v20 offset:swizzle(SWAP,4)
	s_waitcnt lgkmcnt(0)
	v_add_f32_e32 v20, v20, v21
	ds_swizzle_b32 v21, v20 offset:swizzle(SWAP,8)
	s_waitcnt lgkmcnt(0)
	v_add_f32_e32 v20, v20, v21
	ds_swizzle_b32 v21, v20 offset:swizzle(SWAP,16)
	s_waitcnt lgkmcnt(0)
; template <bool FINAL> ...
;     ...
;         const float mean = wave_sum(s) * (1.0f / DM); float q = 0.f;
; #pragma unroll
;         for (int i = 0; i < 32; ++i) { const float d = v[i] - mean; q += d * d; }
;         const float rstd = rsqrtf(wave_sum(q) * (1.0f / DM) + 1e-5f);
	v_add_f32_e32 v20, v20, v21
	v_mov_b32_e32 v21, v20
	s_nop 1
	v_permlane32_swap_b32_e32 v20, v21
	v_add_f32_e32 v20, v20, v21
	v_fmac_f32_e32 v92, 0xba000000, v20
	v_fmac_f32_e32 v91, 0xba000000, v20
	v_mul_f32_e32 v21, v92, v92
	v_fmac_f32_e32 v21, v91, v91
	v_fmac_f32_e32 v86, 0xba000000, v20
	v_fmac_f32_e32 v21, v86, v86
	v_fmac_f32_e32 v88, 0xba000000, v20
	v_fmac_f32_e32 v21, v88, v88
	v_fmac_f32_e32 v93, 0xba000000, v20
	v_fmac_f32_e32 v21, v93, v93
	v_fmac_f32_e32 v95, 0xba000000, v20
	v_fmac_f32_e32 v21, v95, v95
	v_fmac_f32_e32 v100, 0xba000000, v20
	v_fmac_f32_e32 v21, v100, v100
	v_fmac_f32_e32 v102, 0xba000000, v20
	v_fmac_f32_e32 v21, v102, v102
	v_fmac_f32_e32 v32, 0xba000000, v20
	v_fmac_f32_e32 v21, v32, v32
	v_fmac_f32_e32 v33, 0xba000000, v20
	v_fmac_f32_e32 v21, v33, v33
	v_fmac_f32_e32 v82, 0xba000000, v20
	v_fmac_f32_e32 v21, v82, v82
	v_fmac_f32_e32 v84, 0xba000000, v20
	v_fmac_f32_e32 v21, v84, v84
	v_fmac_f32_e32 v87, 0xba000000, v20
	v_fmac_f32_e32 v21, v87, v87
	v_fmac_f32_e32 v89, 0xba000000, v20
	v_fmac_f32_e32 v21, v89, v89
	v_fmac_f32_e32 v97, 0xba000000, v20
	v_fmac_f32_e32 v21, v97, v97
	v_fmac_f32_e32 v98, 0xba000000, v20
	v_fmac_f32_e32 v21, v98, v98
	v_fmac_f32_e32 v34, 0xba000000, v20
	v_fmac_f32_e32 v21, v34, v34
	v_fmac_f32_e32 v35, 0xba000000, v20
	v_fmac_f32_e32 v21, v35, v35
	v_fmac_f32_e32 v74, 0xba000000, v20
	v_fmac_f32_e32 v21, v74, v74
	v_fmac_f32_e32 v83, 0xba000000, v20
	v_fmac_f32_e32 v21, v83, v83
	v_fmac_f32_e32 v85, 0xba000000, v20
	v_fmac_f32_e32 v21, v85, v85
	v_fmac_f32_e32 v94, 0xba000000, v20
	v_fmac_f32_e32 v21, v94, v94
	v_fmac_f32_e32 v99, 0xba000000, v20
	v_fmac_f32_e32 v21, v99, v99
	v_fmac_f32_e32 v101, 0xba000000, v20
	v_fmac_f32_e32 v21, v101, v101
	v_fmac_f32_e32 v72, 0xba000000, v20
	v_fmac_f32_e32 v21, v72, v72
	v_fmac_f32_e32 v73, 0xba000000, v20
	v_fmac_f32_e32 v21, v73, v73
	v_fmac_f32_e32 v75, 0xba000000, v20
	v_fmac_f32_e32 v21, v75, v75
	v_fmac_f32_e32 v78, 0xba000000, v20
	v_fmac_f32_e32 v21, v78, v78
	v_fmac_f32_e32 v80, 0xba000000, v20
	v_fmac_f32_e32 v21, v80, v80
	v_fmac_f32_e32 v96, 0xba000000, v20
	v_fmac_f32_e32 v21, v96, v96
	v_fmac_f32_e32 v79, 0xba000000, v20
	v_fmac_f32_e32 v21, v79, v79
	v_fmac_f32_e32 v76, 0xba000000, v20
	v_fmac_f32_e32 v21, v76, v76
	ds_swizzle_b32 v20, v21 offset:swizzle(SWAP,1)
	s_waitcnt lgkmcnt(0)
	v_add_f32_e32 v20, v21, v20
	ds_swizzle_b32 v21, v20 offset:swizzle(SWAP,2)
	s_waitcnt lgkmcnt(0)
	v_add_f32_e32 v20, v20, v21
	ds_swizzle_b32 v21, v20 offset:swizzle(SWAP,4)
	s_waitcnt lgkmcnt(0)
	v_add_f32_e32 v20, v20, v21
	ds_swizzle_b32 v21, v20 offset:swizzle(SWAP,8)
	s_waitcnt lgkmcnt(0)
	v_add_f32_e32 v20, v20, v21
	ds_swizzle_b32 v21, v20 offset:swizzle(SWAP,16)
	s_waitcnt lgkmcnt(0)
	v_add_f32_e32 v20, v20, v21
	v_mov_b32_e32 v21, v20
	s_nop 1
	v_permlane32_swap_b32_e32 v20, v21
	v_add_f32_e32 v20, v20, v21
	v_mov_b32_e32 v21, 0x3727c5ac
	v_fmamk_f32 v20, v20, 0x3a000000, v21
	v_cmp_gt_f32_e32 vcc, s91, v20
	v_mul_f32_e32 v21, 0x4b800000, v20
	s_nop 0
	v_cndmask_b32_e32 v20, v20, v21, vcc
	v_rsq_f32_e32 v20, v20
	s_nop 0
	v_mul_f32_e32 v21, 0x45800000, v20
	v_cndmask_b32_e32 v77, v20, v21, vcc
	s_nop 0
	s_nop 0
	s_nop 0
	s_nop 0
	v_mul_f32_e32 v81, v91, v77
	v_mul_f32_e32 v34, v34, v77
	s_waitcnt vmcnt(0)
; __device__ __forceinline__ unsigned cvtpk(float lo, float hi) { unsigned r; asm volatile("v_cvt_pk_bf16_f32 %0, %1, %2" : "=v"(r) : "v"(lo), "v"(hi)); return r; }
; template <bool FINAL> ...
;     ...
; #pragma unroll
;         for (int i = 0; i < 4; ++i) { const int col = 8 * lane + 512 * i;
;             const f32x4 ga = *(const f32x4*)(g + col), gb = *(const f32x4*)(g + col + 4), ba = *(const f32x4*)(bb + col), bbv = *(const f32x4*)(bb + col + 4);
;             float y[8];
; #pragma unroll
;             for (int j = 0; j < 4; ++j) { y[j] = (v[i * 8 + j] - mean) * rstd * ga[j] + ba[j]; y[4 + j] = (v[i * 8 + 4 + j] - mean) * rstd * gb[j] + bbv[j]; }
;     ...
;             if (dbg_bad) { for (int j = 0; j < 8; ++j) y[j] = 0.f; }
;     ...
;             if constexpr (FINAL) { *(f32x4*)(fo + (size_t)m * DM + col) = (f32x4){y[0], y[1], y[2], y[3]}; *(f32x4*)(fo + (size_t)m * DM + col + 4) = (f32x4){y[4], y[5], y[6], y[7]}; }
;             else { *(u32x4*)(xo + (size_t)m * DM + col) = (u32x4){cvtpk(y[0], y[1]), cvtpk(y[2], y[3]), cvtpk(y[4], y[5]), cvtpk(y[6], y[7])};
;                 if constexpr (F8_IN) *(u32x2*)(xq + (size_t)m * DM + col) = (u32x2){pk4_fp8(y[0], y[1], y[2], y[3]), pk4_fp8(y[4], y[5], y[6], y[7])}; } }
	v_fma_f32 v108, v180, v81, v188
	v_mul_f32_e32 v28, v93, v77
	v_fma_f32 v109, v176, v28, v184
	v_mul_f32_e32 v20, v92, v77
	v_fma_f32 v28, v181, v20, v189
	v_mul_f32_e32 v20, v95, v77
	v_fma_f32 v29, v177, v20, v185
	v_mul_f32_e32 v20, v86, v77
	v_fma_f32 v30, v182, v20, v190
	v_mul_f32_e32 v20, v100, v77
	v_fma_f32 v26, v178, v20, v186
	v_mul_f32_e32 v20, v88, v77
	v_fma_f32 v31, v183, v20, v191
	v_mul_f32_e32 v20, v102, v77
	v_fma_f32 v27, v179, v20, v187
	v_cvt_pk_bf16_f32 v22, v108, v28
	v_cvt_pk_bf16_f32 v23, v30, v31
	v_cvt_pk_bf16_f32 v24, v109, v29
	v_cvt_pk_fp8_f32 v108, v108, v28
	v_cvt_pk_fp8_f32 v109, v109, v29
	v_lshl_add_u64 v[20:21], s[2:3], 0, v[232:233]
	v_add_co_u32_e32 v20, vcc, s0, v20
	v_cvt_pk_fp8_f32 v108, v30, v31 op_sel:[0,0,1]
	v_cvt_pk_fp8_f32 v109, v26, v27 op_sel:[0,0,1]
	v_addc_co_u32_e32 v21, vcc, 0, v21, vcc
	v_cvt_pk_bf16_f32 v25, v26, v27
	global_store_dwordx4 v[20:21], v[22:25], off
	global_store_dwordx2 v[50:51], v[108:109], off
	s_nop 0
	s_nop 0
	s_nop 0
	s_nop 0
	s_nop 0
	v_mul_f32_e32 v30, v32, v77
	v_readlane_b32 s0, v255, 29
	v_readlane_b32 s1, v255, 30
	v_fma_f32 v30, v30, v196, v212
	v_mul_f32_e32 v26, v87, v77
	v_fma_f32 v31, v26, v192, v200
	v_mul_f32_e32 v22, v33, v77
	v_fma_f32 v26, v22, v197, v213
	v_mul_f32_e32 v22, v89, v77
	v_fma_f32 v27, v22, v193, v201
	v_mul_f32_e32 v22, v82, v77
	v_fma_f32 v28, v22, v198, v214
	v_mul_f32_e32 v22, v97, v77
	v_fma_f32 v32, v22, v194, v202
	v_mul_f32_e32 v22, v84, v77
	v_fma_f32 v109, v22, v199, v215
	v_mul_f32_e32 v22, v98, v77
	v_fma_f32 v105, v22, v195, v203
	v_cvt_pk_bf16_f32 v22, v30, v26
	v_cvt_pk_bf16_f32 v23, v28, v109
	v_cvt_pk_bf16_f32 v24, v31, v27
	v_cvt_pk_fp8_f32 v30, v30, v26
	v_cvt_pk_fp8_f32 v31, v31, v27
	v_cvt_pk_bf16_f32 v25, v32, v105
	global_store_dwordx4 v[20:21], v[22:25], off offset:1024
	v_cvt_pk_fp8_f32 v30, v28, v109 op_sel:[0,0,1]
	v_cvt_pk_fp8_f32 v31, v32, v105 op_sel:[0,0,1]
	global_store_dwordx2 v[50:51], v[30:31], off offset:512
	s_nop 0
	s_nop 0
	s_nop 0
	s_nop 0
	s_nop 0
	v_fma_f32 v84, v34, v148, v156
	v_mul_f32_e32 v26, v85, v77
	v_fma_f32 v85, v26, v144, v152
	v_mul_f32_e32 v22, v35, v77
	v_fma_f32 v26, v22, v149, v157
	v_mul_f32_e32 v22, v94, v77
	v_fma_f32 v27, v22, v145, v153
	v_mul_f32_e32 v22, v74, v77
	v_fma_f32 v28, v22, v150, v158
	v_mul_f32_e32 v22, v99, v77
	v_fma_f32 v30, v22, v146, v154
	v_mul_f32_e32 v22, v83, v77
	v_fma_f32 v89, v22, v151, v159
	v_mul_f32_e32 v22, v101, v77
	v_fma_f32 v33, v22, v147, v155
	v_cvt_pk_bf16_f32 v22, v84, v26
	v_cvt_pk_bf16_f32 v23, v28, v89
	v_cvt_pk_bf16_f32 v24, v85, v27
	v_cvt_pk_fp8_f32 v84, v84, v26
	v_cvt_pk_fp8_f32 v85, v85, v27
	v_cvt_pk_bf16_f32 v25, v30, v33
	global_store_dwordx4 v[20:21], v[22:25], off offset:2048
	v_cvt_pk_fp8_f32 v84, v28, v89 op_sel:[0,0,1]
	v_cvt_pk_fp8_f32 v85, v30, v33 op_sel:[0,0,1]
	v_mul_f32_e32 v34, v72, v77
	v_mov_b64_e32 v[86:87], v[52:53]
	v_mov_b64_e32 v[88:89], v[60:61]
	global_store_dwordx2 v[50:51], v[84:85], off offset:1024
	s_nop 0
	s_nop 0
	s_nop 0
	s_nop 0
	s_nop 0
	v_fma_f32 v34, v34, v168, v204
	v_mul_f32_e32 v26, v80, v77
	v_fma_f32 v35, v26, v160, v172
	v_mul_f32_e32 v22, v73, v77
	v_fma_f32 v26, v22, v169, v205
	v_mul_f32_e32 v22, v96, v77
	v_fma_f32 v27, v22, v161, v173
	v_mul_f32_e32 v22, v75, v77
	v_fma_f32 v28, v22, v170, v206
	v_mul_f32_e32 v22, v79, v77
	v_fma_f32 v30, v22, v162, v174
	v_mul_f32_e32 v22, v78, v77
	v_fma_f32 v85, v22, v171, v207
	v_mul_f32_e32 v22, v76, v77
	v_fma_f32 v33, v22, v163, v175
	v_cvt_pk_bf16_f32 v22, v34, v26
	v_cvt_pk_bf16_f32 v23, v28, v85
	v_cvt_pk_bf16_f32 v24, v35, v27
	v_cvt_pk_fp8_f32 v34, v34, v26
	v_cvt_pk_fp8_f32 v35, v35, v27
	v_cvt_pk_bf16_f32 v25, v30, v33
	global_store_dwordx4 v[20:21], v[22:25], off offset:3072
	v_cvt_pk_fp8_f32 v34, v28, v85 op_sel:[0,0,1]
	v_cvt_pk_fp8_f32 v35, v30, v33 op_sel:[0,0,1]
	v_mov_b64_e32 v[30:31], v[10:11]
	v_mov_b64_e32 v[26:27], v[14:15]
	v_mov_b64_e32 v[22:23], v[18:19]
	global_store_dwordx2 v[50:51], v[34:35], off offset:1536
	v_lshl_add_u64 v[50:51], v[50:51], 0, s[0:1]
	v_readlane_b32 s0, v255, 25
	v_readlane_b32 s1, v255, 26
	s_add_u32 s2, s2, s0
	s_addc_u32 s3, s3, s1
	s_add_i32 s34, s34, s80
	s_add_u32 s38, s38, s0
	v_mov_b64_e32 v[34:35], v[6:7]
	s_addc_u32 s39, s39, s1
	s_and_b64 vcc, exec, s[40:41]
	v_mov_b64_e32 v[32:33], v[4:5]
	v_mov_b64_e32 v[28:29], v[8:9]
	v_mov_b64_e32 v[24:25], v[12:13]
	v_mov_b64_e32 v[20:21], v[16:17]
	v_mov_b64_e32 v[82:83], v[54:55]
	v_mov_b64_e32 v[72:73], v[56:57]
	v_mov_b64_e32 v[78:79], v[58:59]
	v_mov_b64_e32 v[84:85], v[62:63]
	v_mov_b64_e32 v[74:75], v[64:65]
	v_mov_b64_e32 v[80:81], v[68:69]
	s_mov_b32 s0, s6
	v_mov_b64_e32 v[76:77], v[66:67]
	s_cbranch_vccnz .LBB0_1111
